# MoE main K loops: weight-tile loads addressed from scalar bases, each k-row pair's loads issued right behind its conversions
# baseline (speedup 1.0000x reference)
; #define MG_STAGE_A(b, rows, k0) do { _Pragma("unroll") for (int h_ = 0; h_ < 2; ++h_) _Pragma("unroll") for (int i_ = 0; i_ < 2; ++i_) if (rows[h_][i_] != 0xffffffffu) \
;         __builtin_amdgcn_global_load_lds((const unsigned*)((const char*)Abase + rows[h_][i_] + (k0) * 2), (PG8_LAS unsigned*)(lds + MG_SA(b, h_) + ldsw + i_ * 8192), 16, 0, 0); } while (0)
; #define MG_LOAD_B(ptr, k0) do { _Pragma("unroll") for (int j_ = 0; j_ < 8; ++j_) bv[j_] = *(const f32x4*)((ptr) + (size_t)((k0) + j_) * LDW); } while (0)
; #define MG_WRITE_B(b) do { _Pragma("unroll") for (int c_ = 0; c_ < 4; ++c_) { u32x4 w_; w_.x = cvt_pk_bf16(bv[0][c_], bv[1][c_]); w_.y = cvt_pk_bf16(bv[2][c_], bv[3][c_]); w_.z = cvt_pk_bf16(bv[4][c_], bv[5][c_]); w_.w = cvt_pk_bf16(bv[6][c_], bv[7][c_]); \
;         *(PG8_LAS u32x4*)(lds + MG_SB(b, hfB) + wB0 + 64 * c_) = w_; } } while (0)
; template <class Epi, bool G1> ...
;     ...
;     MG_ROWS(cur, rowC); const float* bC = MG_BPTR(cur); bool bact = MG_BACT(cur);
;     MG_STAGE_A(0, rowC, 0); if (bact) { MG_LOAD_B(bC, 0); MG_WRITE_B(0); }
.LBB0_1073:
	v_mov_b32_e32 v199, v197
	v_mov_b32_e32 v193, v197
	v_mov_b32_e32 v195, v197
	s_xor_b64 s[38:39], s[40:41], -1
	v_lshl_add_u64 v[206:207], v[196:197], 0, s[30:31]
	v_lshl_add_u64 v[208:209], v[198:199], 0, s[30:31]
	v_lshl_add_u64 v[210:211], v[192:193], 0, s[30:31]
	v_lshl_add_u64 v[212:213], v[194:195], 0, s[30:31]
	v_cmp_ne_u32_e64 s[14:15], -1, v194
	v_cmp_ne_u32_e64 s[12:13], -1, v192
	v_cmp_ne_u32_e64 s[8:9], -1, v198
	v_cmp_ne_u32_e64 s[6:7], -1, v196
	v_readfirstlane_b32 s88, v200
	v_readfirstlane_b32 s89, v201
	s_nop 1
	v_subrev_u32_e32 v245, s88, v200
	v_mbcnt_lo_u32_b32 v226, -1, 0
	v_mbcnt_hi_u32_b32 v226, -1, v226
	v_lshl_add_u32 v226, v226, 4, s51
	v_mov_b32_e32 v228, 0
	v_mov_b32_e32 v229, 0
	v_mov_b32_e32 v230, 0
	v_mov_b32_e32 v231, 0
	s_andn2_b64 exec, exec, s[14:15]
	ds_write_b128 v226, v[228:231]
	ds_write_b128 v226, v[228:231] offset:32768
	s_mov_b64 exec, -1
	s_andn2_b64 exec, exec, s[12:13]
	ds_write_b128 v226, v[228:231] offset:8192
	ds_write_b128 v226, v[228:231] offset:40960
	s_mov_b64 exec, -1
	s_andn2_b64 exec, exec, s[8:9]
	ds_write_b128 v226, v[228:231] offset:16384
	ds_write_b128 v226, v[228:231] offset:49152
	s_mov_b64 exec, -1
	s_andn2_b64 exec, exec, s[6:7]
	ds_write_b128 v226, v[228:231] offset:24576
	ds_write_b128 v226, v[228:231] offset:57344
	s_mov_b64 exec, -1
	s_mov_b64 s[42:43], 0
	s_mov_b64 s[44:45], s[2:3]
	s_branch .LBB0_1075

; #define MG_LOAD_B(ptr, k0) do { _Pragma("unroll") for (int j_ = 0; j_ < 8; ++j_) bv[j_] = *(const f32x4*)((ptr) + (size_t)((k0) + j_) * LDW); } while (0)
; #define MG_WRITE_B(b) do { _Pragma("unroll") for (int c_ = 0; c_ < 4; ++c_) { u32x4 w_; w_.x = cvt_pk_bf16(bv[0][c_], bv[1][c_]); w_.y = cvt_pk_bf16(bv[2][c_], bv[3][c_]); w_.z = cvt_pk_bf16(bv[4][c_], bv[5][c_]); w_.w = cvt_pk_bf16(bv[6][c_], bv[7][c_]); \
;         *(PG8_LAS u32x4*)(lds + MG_SB(b, hfB) + wB0 + 64 * c_) = w_; } } while (0)
; template <class Epi, bool G1> ...
;     ...
;             if (more && bactP) MG_WRITE_B(buf ^ 1);
;             bool issued = false;
;             if (t + 2 < NT) { if (bact) MG_LOAD_B(bC, (t + 2) * BK); issued = true; }
;             else if (has_next) { if (t + 2 == NT) { bC = MG_BPTR(nxt); bact = MG_BACT(nxt); } if (bact) MG_LOAD_B(bC, (t + 2 - NT) * BK); issued = true; }
.LBB0_1088:
	s_lshl_b32 s73, s70, 1
	s_xor_b32 s73, s73, 2
	s_add_i32 s73, s73, s55
	v_lshl_add_u32 v203, s73, 14, v220
	s_add_u32 s90, s88, s42
	s_addc_u32 s91, s89, s43
	s_add_u32 s90, s90, 0x81000
	s_addc_u32 s91, s91, 0
	s_add_u32 s92, s90, 0x2000
	s_addc_u32 s93, s91, 0
	s_add_u32 s94, s92, 0x2000
	s_addc_u32 s95, s93, 0
	s_add_u32 s98, s94, 0x2000
	s_addc_u32 s99, s95, 0
	s_waitcnt vmcnt(0)
	v_cvt_pk_bf16_f32 v226, v12, v0
	v_cvt_pk_bf16_f32 v230, v13, v1
	v_cvt_pk_bf16_f32 v234, v14, v2
	v_cvt_pk_bf16_f32 v238, v15, v3
	global_load_dwordx4 v[12:15], v245, s[90:91] offset:-4096
	global_load_dwordx4 v[0:3], v245, s[90:91]
	v_cvt_pk_bf16_f32 v227, v4, v8
	v_cvt_pk_bf16_f32 v231, v5, v9
	v_cvt_pk_bf16_f32 v235, v6, v10
	v_cvt_pk_bf16_f32 v239, v7, v11
	global_load_dwordx4 v[4:7], v245, s[92:93] offset:-4096
	global_load_dwordx4 v[8:11], v245, s[92:93]
	v_cvt_pk_bf16_f32 v228, v16, v20
	v_cvt_pk_bf16_f32 v232, v17, v21
	v_cvt_pk_bf16_f32 v236, v18, v22
	v_cvt_pk_bf16_f32 v240, v19, v23
	global_load_dwordx4 v[16:19], v245, s[94:95] offset:-4096
	global_load_dwordx4 v[20:23], v245, s[94:95]
	v_cvt_pk_bf16_f32 v229, v28, v44
	v_cvt_pk_bf16_f32 v233, v29, v45
	v_cvt_pk_bf16_f32 v237, v30, v46
	v_cvt_pk_bf16_f32 v241, v31, v47
	global_load_dwordx4 v[28:31], v245, s[98:99] offset:-4096
	global_load_dwordx4 v[44:47], v245, s[98:99]
	ds_write_b128 v203, v[226:229]
	ds_write_b128 v203, v[230:233] offset:64
	ds_write_b128 v203, v[234:237] offset:128
	ds_write_b128 v203, v[238:241] offset:192
	s_branch .LBB0_1074

; #define MG_STAGE_A(b, rows, k0) do { _Pragma("unroll") for (int h_ = 0; h_ < 2; ++h_) _Pragma("unroll") for (int i_ = 0; i_ < 2; ++i_) if (rows[h_][i_] != 0xffffffffu) \
;         __builtin_amdgcn_global_load_lds((const unsigned*)((const char*)Abase + rows[h_][i_] + (k0) * 2), (PG8_LAS unsigned*)(lds + MG_SA(b, h_) + ldsw + i_ * 8192), 16, 0, 0); } while (0)
; #define MG_LOAD_B(ptr, k0) do { _Pragma("unroll") for (int j_ = 0; j_ < 8; ++j_) bv[j_] = *(const f32x4*)((ptr) + (size_t)((k0) + j_) * LDW); } while (0)
; #define MG_WRITE_B(b) do { _Pragma("unroll") for (int c_ = 0; c_ < 4; ++c_) { u32x4 w_; w_.x = cvt_pk_bf16(bv[0][c_], bv[1][c_]); w_.y = cvt_pk_bf16(bv[2][c_], bv[3][c_]); w_.z = cvt_pk_bf16(bv[4][c_], bv[5][c_]); w_.w = cvt_pk_bf16(bv[6][c_], bv[7][c_]); \
;         *(PG8_LAS u32x4*)(lds + MG_SB(b, hfB) + wB0 + 64 * c_) = w_; } } while (0)
; template <class Epi, bool G1> ...
;     ...
;     MG_ROWS(cur, rowC); const float* bC = MG_BPTR(cur); bool bact = MG_BACT(cur);
;     MG_STAGE_A(0, rowC, 0); if (bact) { MG_LOAD_B(bC, 0); MG_WRITE_B(0); }
.LBB0_1262:
	v_mov_b32_e32 v203, v1
	v_mov_b32_e32 v201, v1
	v_mov_b32_e32 v199, v1
	s_xor_b64 s[16:17], s[46:47], -1
	v_lshl_add_u64 v[2:3], v[0:1], 0, s[40:41]
	v_lshl_add_u64 v[208:209], v[202:203], 0, s[40:41]
	v_lshl_add_u64 v[210:211], v[200:201], 0, s[40:41]
	v_lshl_add_u64 v[212:213], v[198:199], 0, s[40:41]
	v_cmp_ne_u32_e64 s[14:15], -1, v198
	v_cmp_ne_u32_e64 s[12:13], -1, v200
	v_cmp_ne_u32_e64 s[8:9], -1, v202
	v_cmp_ne_u32_e64 s[6:7], -1, v0
	v_readfirstlane_b32 s88, v196
	v_readfirstlane_b32 s89, v197
	s_nop 1
	v_subrev_u32_e32 v245, s88, v196
	v_add_u32_e32 v246, 0x2000, v245
	v_mbcnt_lo_u32_b32 v226, -1, 0
	v_mbcnt_hi_u32_b32 v226, -1, v226
	v_lshl_add_u32 v226, v226, 4, s57
	v_mov_b32_e32 v228, 0
	v_mov_b32_e32 v229, 0
	v_mov_b32_e32 v230, 0
	v_mov_b32_e32 v231, 0
	s_andn2_b64 exec, exec, s[14:15]
	ds_write_b128 v226, v[228:231]
	ds_write_b128 v226, v[228:231] offset:32768
	s_mov_b64 exec, -1
	s_andn2_b64 exec, exec, s[12:13]
	ds_write_b128 v226, v[228:231] offset:8192
	ds_write_b128 v226, v[228:231] offset:40960
	s_mov_b64 exec, -1
	s_andn2_b64 exec, exec, s[8:9]
	ds_write_b128 v226, v[228:231] offset:16384
	ds_write_b128 v226, v[228:231] offset:49152
	s_mov_b64 exec, -1
	s_andn2_b64 exec, exec, s[6:7]
	ds_write_b128 v226, v[228:231] offset:24576
	ds_write_b128 v226, v[228:231] offset:57344
	s_mov_b64 exec, -1
	s_mov_b64 s[48:49], 0
	s_mov_b64 s[50:51], s[18:19]
	s_branch .LBB0_1264

; #define MG_LOAD_B(ptr, k0) do { _Pragma("unroll") for (int j_ = 0; j_ < 8; ++j_) bv[j_] = *(const f32x4*)((ptr) + (size_t)((k0) + j_) * LDW); } while (0)
; #define MG_WRITE_B(b) do { _Pragma("unroll") for (int c_ = 0; c_ < 4; ++c_) { u32x4 w_; w_.x = cvt_pk_bf16(bv[0][c_], bv[1][c_]); w_.y = cvt_pk_bf16(bv[2][c_], bv[3][c_]); w_.z = cvt_pk_bf16(bv[4][c_], bv[5][c_]); w_.w = cvt_pk_bf16(bv[6][c_], bv[7][c_]); \
;         *(PG8_LAS u32x4*)(lds + MG_SB(b, hfB) + wB0 + 64 * c_) = w_; } } while (0)
; template <class Epi, bool G1> ...
;     ...
;             if (more && bactP) MG_WRITE_B(buf ^ 1);
;             bool issued = false;
;             if (t + 2 < NT) { if (bact) MG_LOAD_B(bC, (t + 2) * BK); issued = true; }
;             else if (has_next) { if (t + 2 == NT) { bC = MG_BPTR(nxt); bact = MG_BACT(nxt); } if (bact) MG_LOAD_B(bC, (t + 2 - NT) * BK); issued = true; }
.LBB0_1277:
	s_lshl_b32 s76, s73, 1
	s_xor_b32 s76, s76, 2
	s_add_i32 s76, s76, s59
	v_lshl_add_u32 v205, s76, 14, v222
	s_add_u32 s90, s88, s48
	s_addc_u32 s91, s89, s49
	s_add_u32 s90, s90, 0x100000
	s_addc_u32 s91, s91, 0
	s_add_u32 s92, s90, 0x4000
	s_addc_u32 s93, s91, 0
	s_add_u32 s94, s92, 0x4000
	s_addc_u32 s95, s93, 0
	s_add_u32 s98, s94, 0x4000
	s_addc_u32 s99, s95, 0
	s_waitcnt vmcnt(0)
	v_cvt_pk_bf16_f32 v226, v12, v4
	v_cvt_pk_bf16_f32 v230, v13, v5
	v_cvt_pk_bf16_f32 v234, v14, v6
	v_cvt_pk_bf16_f32 v238, v15, v7
	global_load_dwordx4 v[12:15], v245, s[90:91]
	global_load_dwordx4 v[4:7], v246, s[90:91]
	v_cvt_pk_bf16_f32 v227, v8, v16
	v_cvt_pk_bf16_f32 v231, v9, v17
	v_cvt_pk_bf16_f32 v235, v10, v18
	v_cvt_pk_bf16_f32 v239, v11, v19
	global_load_dwordx4 v[8:11], v245, s[92:93]
	global_load_dwordx4 v[16:19], v246, s[92:93]
	v_cvt_pk_bf16_f32 v228, v20, v24
	v_cvt_pk_bf16_f32 v232, v21, v25
	v_cvt_pk_bf16_f32 v236, v22, v26
	v_cvt_pk_bf16_f32 v240, v23, v27
	global_load_dwordx4 v[20:23], v245, s[94:95]
	global_load_dwordx4 v[24:27], v246, s[94:95]
	v_cvt_pk_bf16_f32 v229, v28, v56
	v_cvt_pk_bf16_f32 v233, v29, v57
	v_cvt_pk_bf16_f32 v237, v30, v58
	v_cvt_pk_bf16_f32 v241, v31, v59
	global_load_dwordx4 v[28:31], v245, s[98:99]
	global_load_dwordx4 v[56:59], v246, s[98:99]
	ds_write_b128 v205, v[226:229]
	ds_write_b128 v205, v[230:233] offset:64
	ds_write_b128 v205, v[234:237] offset:128
	ds_write_b128 v205, v[238:241] offset:192
	s_branch .LBB0_1263
